# pool mixer: the 8 conditional old-row loads no longer wait one by one (loads into pre-zeroed registers, one wait, unpack afterwards)
# baseline (speedup 1.0000x reference)
; __global__ void __launch_bounds__(NWAVES * 64, 2) mk_fwd(Args args) {
;     ...
;                 for (int rb = r0; rb < r0 + 32; rb += 8) {
;                     f32x4 cur8[8], old8[8];
; #pragma unroll
;                     for (int i = 0; i < 8; ++i) { const int r = rb + i, lo = r - wsz + 1;
;                         cur8[i] = XLD4(xc + XIDX(r, c));
;                         old8[i] = lo >= 0 ? XLD4(xc + XIDX(lo, c)) : (f32x4){0.f, 0.f, 0.f, 0.f}; }
.LBB0_292:
	v_mov_b32_e32 v112, 0
	v_mov_b32_e32 v113, 0
	v_mov_b32_e32 v114, 0
	v_mov_b32_e32 v115, 0
	v_mov_b32_e32 v116, 0
	v_mov_b32_e32 v117, 0
	v_mov_b32_e32 v118, 0
	v_mov_b32_e32 v119, 0
	v_mov_b32_e32 v120, 0
	v_mov_b32_e32 v121, 0
	v_mov_b32_e32 v122, 0
	v_mov_b32_e32 v123, 0
	v_mov_b32_e32 v124, 0
	v_mov_b32_e32 v125, 0
	v_mov_b32_e32 v126, 0
	v_mov_b32_e32 v127, 0
	s_add_i32 s43, s41, -8
	s_ashr_i32 s8, s43, 3
	s_andn2_b32 s8, s8, 31
	v_add_u32_e32 v16, s8, v36
	v_readlane_b32 s8, v251, 56
	v_ashrrev_i32_e32 v17, 31, v16
	s_add_i32 s45, s8, s39
	v_lshlrev_b64 v[16:17], 15, v[16:17]
	s_and_b32 s8, s45, 0x3e00
	v_lshl_add_u64 v[16:17], v[12:13], 0, v[16:17]
	s_lshl_b32 s80, s8, 1
	v_lshl_add_u64 v[18:19], v[16:17], 0, s[80:81]
	global_load_dwordx2 v[30:31], v[18:19], off
	v_add_u32_e32 v83, s41, v42
	v_add_u32_e32 v81, -8, v83
	s_mov_b32 s13, s81
	v_cmp_lt_i32_e64 s[22:23], -2, v81
	v_mov_b32_e32 v76, 0
	v_add_u32_e32 v82, s39, v41
	v_lshlrev_b32_e32 v32, 1, v10
	v_mov_b32_e32 v78, 0
	v_mov_b32_e32 v79, 0
	v_mov_b32_e32 v80, 0
	s_and_saveexec_b64 s[8:9], s[22:23]
	s_cbranch_execz .LBB0_294
	v_lshrrev_b32_e32 v18, 3, v81
	v_and_b32_e32 v18, 0x1fffffe0, v18
	v_add_u32_e32 v18, v18, v36
	v_ashrrev_i32_e32 v19, 31, v18
	v_and_b32_e32 v20, 0x3f80, v82
	v_lshlrev_b64 v[18:19], 15, v[18:19]
	v_lshl_add_u64 v[18:19], s[0:1], 0, v[18:19]
	v_lshlrev_b32_e32 v128, 1, v20
	v_lshl_add_u64 v[18:19], v[18:19], 0, v[128:129]
	v_mov_b32_e32 v33, v129
	v_lshl_add_u64 v[18:19], v[18:19], 0, v[32:33]
	global_load_dwordx2 v[112:113], v[18:19], off offset:128
.LBB0_294:
	s_or_b64 exec, exec, s[8:9]
	s_add_i32 s8, s45, 64
	s_and_b32 s8, s8, 0x3e40
	s_mov_b32 s9, s13
	s_lshl_b32 s8, s8, 1
	v_lshl_add_u64 v[18:19], v[16:17], 0, s[8:9]
	global_load_dwordx2 v[28:29], v[18:19], off
	v_add_u32_e32 v74, -7, v83
	v_cmp_lt_i32_e64 s[20:21], -2, v74
	v_cmp_gt_i32_e32 vcc, -1, v74
	v_add_u32_e32 v63, -6, v83
	s_and_saveexec_b64 s[8:9], vcc
	s_xor_b64 s[8:9], exec, s[8:9]
	v_add_u32_e32 v63, -6, v83
	s_or_saveexec_b64 s[8:9], s[8:9]
	v_mov_b32_e32 v60, 0
	v_add_u32_e32 v18, 0x80, v82
	v_mov_b32_e32 v72, 0
	v_mov_b32_e32 v73, 0
	v_mov_b32_e32 v75, 0
	v_mov_b32_e32 v77, 0
	s_xor_b64 exec, exec, s[8:9]
	s_cbranch_execz .LBB0_298
	v_lshrrev_b32_e32 v19, 3, v63
	v_and_b32_e32 v19, 0x1fffffe0, v19
	v_add_u32_e32 v20, v19, v36
	v_ashrrev_i32_e32 v21, 31, v20
	v_and_b32_e32 v19, 0x3f80, v18
	v_lshlrev_b64 v[20:21], 15, v[20:21]
	v_lshl_add_u64 v[20:21], s[0:1], 0, v[20:21]
	v_lshlrev_b32_e32 v128, 1, v19
	v_lshl_add_u64 v[20:21], v[20:21], 0, v[128:129]
	v_mov_b32_e32 v33, v129
	v_lshl_add_u64 v[20:21], v[20:21], 0, v[32:33]
	global_load_dwordx2 v[114:115], v[20:21], off
.LBB0_298:
	s_or_b64 exec, exec, s[8:9]
	s_add_i32 s8, s45, 0x80
	s_and_b32 s8, s8, 0x3e80
	s_mov_b32 s9, s13
	s_lshl_b32 s8, s8, 1
	v_lshl_add_u64 v[20:21], v[16:17], 0, s[8:9]
	global_load_dwordx2 v[26:27], v[20:21], off
	v_cmp_lt_i32_e64 s[18:19], -2, v63
	v_mov_b32_e32 v69, 0
	v_mov_b32_e32 v70, 0
	v_mov_b32_e32 v71, 0
	s_and_saveexec_b64 s[8:9], s[18:19]
	s_cbranch_execz .LBB0_300
	v_lshrrev_b32_e32 v19, 3, v63
	v_and_b32_e32 v19, 0x1fffffe0, v19
	v_add_u32_e32 v20, v19, v36
	v_ashrrev_i32_e32 v21, 31, v20
	v_and_b32_e32 v22, 0x3f80, v18
	v_lshlrev_b64 v[18:19], 15, v[20:21]
	v_lshl_add_u64 v[18:19], s[0:1], 0, v[18:19]
	v_lshlrev_b32_e32 v128, 1, v22
	v_lshl_add_u64 v[18:19], v[18:19], 0, v[128:129]
	v_mov_b32_e32 v33, v129
	v_lshl_add_u64 v[18:19], v[18:19], 0, v[32:33]
	global_load_dwordx2 v[116:117], v[18:19], off offset:128
.LBB0_300:
	s_or_b64 exec, exec, s[8:9]
	s_add_i32 s8, s45, 0xc0
	s_and_b32 s8, s8, 0x3ec0
	s_mov_b32 s9, s13
	s_lshl_b32 s8, s8, 1
	v_lshl_add_u64 v[18:19], v[16:17], 0, s[8:9]
	global_load_dwordx2 v[24:25], v[18:19], off
	v_add_u32_e32 v66, -5, v83
	v_cmp_lt_i32_e64 s[16:17], -2, v66
	v_cmp_gt_i32_e32 vcc, -1, v66
	v_add_u32_e32 v53, -4, v83
	s_and_saveexec_b64 s[8:9], vcc
	s_xor_b64 s[8:9], exec, s[8:9]
	v_add_u32_e32 v53, -4, v83
	s_or_saveexec_b64 s[8:9], s[8:9]
	v_mov_b32_e32 v50, 0
	v_add_u32_e32 v18, 0x100, v82
	v_mov_b32_e32 v64, 0
	v_mov_b32_e32 v65, 0
	v_mov_b32_e32 v67, 0
	v_mov_b32_e32 v68, 0
	s_xor_b64 exec, exec, s[8:9]
	s_cbranch_execz .LBB0_304
	v_lshrrev_b32_e32 v19, 3, v53
	v_and_b32_e32 v19, 0x1fffffe0, v19
	v_add_u32_e32 v20, v19, v36
	v_ashrrev_i32_e32 v21, 31, v20
	v_and_b32_e32 v19, 0x3f80, v18
	v_lshlrev_b64 v[20:21], 15, v[20:21]
	v_lshl_add_u64 v[20:21], s[0:1], 0, v[20:21]
	v_lshlrev_b32_e32 v128, 1, v19
	v_lshl_add_u64 v[20:21], v[20:21], 0, v[128:129]
	v_mov_b32_e32 v33, v129
	v_lshl_add_u64 v[20:21], v[20:21], 0, v[32:33]
	global_load_dwordx2 v[118:119], v[20:21], off
.LBB0_304:
	s_or_b64 exec, exec, s[8:9]
	s_add_i32 s8, s45, 0x100
	s_and_b32 s8, s8, 0x3f00
	s_mov_b32 s9, s13
	s_lshl_b32 s8, s8, 1
	v_lshl_add_u64 v[20:21], v[16:17], 0, s[8:9]
	global_load_dwordx2 v[22:23], v[20:21], off
	v_cmp_lt_i32_e64 s[14:15], -2, v53
	v_mov_b32_e32 v59, 0
	v_mov_b32_e32 v61, 0
	v_mov_b32_e32 v62, 0
	s_and_saveexec_b64 s[8:9], s[14:15]
	s_cbranch_execz .LBB0_306
	v_lshrrev_b32_e32 v19, 3, v53
	v_and_b32_e32 v19, 0x1fffffe0, v19
	v_add_u32_e32 v20, v19, v36
	v_ashrrev_i32_e32 v21, 31, v20
	v_and_b32_e32 v33, 0x3f80, v18
	v_lshlrev_b64 v[18:19], 15, v[20:21]
	v_lshl_add_u64 v[18:19], s[0:1], 0, v[18:19]
	v_lshlrev_b32_e32 v128, 1, v33
	v_lshl_add_u64 v[18:19], v[18:19], 0, v[128:129]
	v_mov_b32_e32 v33, v129
	v_lshl_add_u64 v[18:19], v[18:19], 0, v[32:33]
	global_load_dwordx2 v[120:121], v[18:19], off offset:128
; __device__ __forceinline__ unsigned cvt_pk_bf16(float lo, float hi) { const f32x2_t v = {lo, hi}; const bf16x2_t b = __builtin_convertvector(v, bf16x2_t); return __builtin_bit_cast(unsigned, b); }
; __global__ void __launch_bounds__(NWAVES * 64, 2) mk_fwd(Args args) {
;     ...
;                 for (int rb = r0; rb < r0 + 32; rb += 8) {
;                     f32x4 cur8[8], old8[8];
; #pragma unroll
;                     for (int i = 0; i < 8; ++i) { const int r = rb + i, lo = r - wsz + 1;
;                         cur8[i] = XLD4(xc + XIDX(r, c));
;                         old8[i] = lo >= 0 ? XLD4(xc + XIDX(lo, c)) : (f32x4){0.f, 0.f, 0.f, 0.f}; }
; #pragma unroll
;                     for (int i = 0; i < 8; ++i) { const int r = rb + i, lo = r - wsz + 1;
;                         const f32x4 cur = cur8[i] * rtab[r - r0 + 15];
;                         sum += cur;
;                         const float icnt = 1.0f / (float)(lo < 0 ? r + 1 : wsz);
;                         const f32x4 pv = g4 * (sum * icnt - cur);
;                         u32x2 o; o.x = pg8::cvt_pk_bf16(pv[0], pv[1]); o.y = pg8::cvt_pk_bf16(pv[2], pv[3]); *(u32x2*)(W_ao + (size_t)r * D + c) = o;
;                         if (lo >= 0) sum -= old8[i] * rtab[lo - r0 + 15]; }
.LBB0_306:
	s_or_b64 exec, exec, s[8:9]
	s_add_i32 s8, s45, 0x140
	s_and_b32 s8, s8, 0x3f40
	s_lshl_b32 s12, s8, 1
	v_lshl_add_u64 v[18:19], v[16:17], 0, s[12:13]
	global_load_dwordx2 v[20:21], v[18:19], off
	v_add_u32_e32 v56, -3, v83
	s_mov_b32 s47, s13
	v_cmp_lt_i32_e64 s[12:13], -2, v56
	v_cmp_gt_i32_e32 vcc, -1, v56
	v_add_u32_e32 v47, -2, v83
	s_and_saveexec_b64 s[8:9], vcc
	s_xor_b64 s[8:9], exec, s[8:9]
	v_add_u32_e32 v47, -2, v83
	s_or_saveexec_b64 s[8:9], s[8:9]
	v_mov_b32_e32 v46, 0
	v_add_u32_e32 v43, 0x180, v82
	v_mov_b32_e32 v54, 0
	v_mov_b32_e32 v55, 0
	v_mov_b32_e32 v57, 0
	v_mov_b32_e32 v58, 0
	s_xor_b64 exec, exec, s[8:9]
	s_cbranch_execz .LBB0_310
	v_lshrrev_b32_e32 v18, 3, v47
	v_and_b32_e32 v18, 0x1fffffe0, v18
	v_add_u32_e32 v18, v18, v36
	v_ashrrev_i32_e32 v19, 31, v18
	v_and_b32_e32 v33, 0x3f80, v43
	v_lshlrev_b64 v[18:19], 15, v[18:19]
	v_lshl_add_u64 v[18:19], s[0:1], 0, v[18:19]
	v_lshlrev_b32_e32 v128, 1, v33
	v_lshl_add_u64 v[18:19], v[18:19], 0, v[128:129]
	v_mov_b32_e32 v33, v129
	v_lshl_add_u64 v[18:19], v[18:19], 0, v[32:33]
	global_load_dwordx2 v[122:123], v[18:19], off
.LBB0_310:
	s_or_b64 exec, exec, s[8:9]
	s_add_i32 s8, s45, 0x180
	s_and_b32 s8, s8, 0x3f80
	s_mov_b32 s9, s47
	s_lshl_b32 s8, s8, 1
	v_lshl_add_u64 v[18:19], v[16:17], 0, s[8:9]
	global_load_dwordx2 v[18:19], v[18:19], off
	v_cmp_lt_i32_e64 s[10:11], -2, v47
	v_mov_b32_e32 v49, 0
	v_mov_b32_e32 v51, 0
	v_mov_b32_e32 v52, 0
	s_and_saveexec_b64 s[8:9], s[10:11]
	s_cbranch_execz .LBB0_312
	v_lshrrev_b32_e32 v33, 3, v47
	v_and_b32_e32 v33, 0x1fffffe0, v33
	v_add_u32_e32 v44, v33, v36
	v_ashrrev_i32_e32 v45, 31, v44
	v_and_b32_e32 v33, 0x3f80, v43
	v_lshlrev_b64 v[44:45], 15, v[44:45]
	v_lshl_add_u64 v[44:45], s[0:1], 0, v[44:45]
	v_lshlrev_b32_e32 v128, 1, v33
	v_lshl_add_u64 v[44:45], v[44:45], 0, v[128:129]
	v_mov_b32_e32 v33, v129
	v_lshl_add_u64 v[44:45], v[44:45], 0, v[32:33]
	global_load_dwordx2 v[124:125], v[44:45], off offset:128
.LBB0_312:
	s_or_b64 exec, exec, s[8:9]
	s_addk_i32 s45, 0x1c0
	s_and_b32 s8, s45, 0x3fc0
	s_mov_b32 s9, s47
	s_lshl_b32 s8, s8, 1
	v_lshl_add_u64 v[16:17], v[16:17], 0, s[8:9]
	global_load_dwordx2 v[16:17], v[16:17], off
	v_add_u32_e32 v48, -1, v83
	s_mov_b32 s81, s47
	v_cmp_lt_i32_e64 s[8:9], -2, v48
	v_mov_b32_e32 v33, 0
	v_mov_b32_e32 v43, 0
	v_mov_b32_e32 v44, 0
	v_mov_b32_e32 v45, 0
	s_and_saveexec_b64 s[66:67], s[8:9]
	s_cbranch_execz .LBB0_314
	v_lshrrev_b32_e32 v33, 3, v83
	v_and_b32_e32 v33, 0x1fffffe0, v33
	v_add_u32_e32 v44, v33, v36
	v_ashrrev_i32_e32 v45, 31, v44
	v_add_u32_e32 v33, 0x200, v82
	v_and_b32_e32 v33, 0x3f80, v33
	v_lshlrev_b64 v[44:45], 15, v[44:45]
	v_lshl_add_u64 v[44:45], s[0:1], 0, v[44:45]
	v_lshlrev_b32_e32 v128, 1, v33
	v_lshl_add_u64 v[44:45], v[44:45], 0, v[128:129]
	v_mov_b32_e32 v33, v129
	v_lshl_add_u64 v[32:33], v[44:45], 0, v[32:33]
	global_load_dwordx2 v[126:127], v[32:33], off
.LBB0_314:
	s_or_b64 exec, exec, s[66:67]
	s_waitcnt vmcnt(0)
	v_lshlrev_b32_e32 v76, 16, v112
	v_and_b32_e32 v78, 0xffff0000, v112
	v_lshlrev_b32_e32 v79, 16, v113
	v_and_b32_e32 v80, 0xffff0000, v113
	v_lshlrev_b32_e32 v72, 16, v114
	v_and_b32_e32 v73, 0xffff0000, v114
	v_lshlrev_b32_e32 v75, 16, v115
	v_and_b32_e32 v77, 0xffff0000, v115
	v_lshlrev_b32_e32 v60, 16, v116
	v_and_b32_e32 v69, 0xffff0000, v116
	v_lshlrev_b32_e32 v70, 16, v117
	v_and_b32_e32 v71, 0xffff0000, v117
	v_lshlrev_b32_e32 v64, 16, v118
	v_and_b32_e32 v65, 0xffff0000, v118
	v_lshlrev_b32_e32 v67, 16, v119
	v_and_b32_e32 v68, 0xffff0000, v119
	v_lshlrev_b32_e32 v50, 16, v120
	v_and_b32_e32 v59, 0xffff0000, v120
	v_lshlrev_b32_e32 v61, 16, v121
	v_and_b32_e32 v62, 0xffff0000, v121
	v_lshlrev_b32_e32 v54, 16, v122
	v_and_b32_e32 v55, 0xffff0000, v122
	v_lshlrev_b32_e32 v57, 16, v123
	v_and_b32_e32 v58, 0xffff0000, v123
	v_lshlrev_b32_e32 v46, 16, v124
	v_and_b32_e32 v49, 0xffff0000, v124
	v_lshlrev_b32_e32 v51, 16, v125
	v_and_b32_e32 v52, 0xffff0000, v125
	v_lshlrev_b32_e32 v33, 16, v126
	v_and_b32_e32 v43, 0xffff0000, v126
	v_lshlrev_b32_e32 v44, 16, v127
	v_and_b32_e32 v45, 0xffff0000, v127
	s_add_i32 s45, s41, -7
	v_mov_b32_e32 v84, s45
	v_cmp_gt_i32_e32 vcc, -1, v81
	v_mov_b32_e32 v32, s35
	ds_read_b32 v32, v32
	v_cndmask_b32_e32 v81, v35, v84, vcc
	v_cvt_f32_i32_e32 v81, v81
	s_waitcnt vmcnt(7)
	v_lshlrev_b32_e32 v82, 16, v30
	v_and_b32_e32 v83, 0xffff0000, v30
	v_lshlrev_b32_e32 v30, 16, v31
	v_div_scale_f32 v88, s[66:67], v81, v81, 1.0
	v_rcp_f32_e32 v89, v88
	v_and_b32_e32 v31, 0xffff0000, v31
	s_waitcnt lgkmcnt(0)
	v_pk_mul_f32 v[84:85], v[32:33], v[30:31] op_sel_hi:[0,1]
	v_pk_fma_f32 v[6:7], v[32:33], v[30:31], v[6:7] op_sel_hi:[0,1,1]
	v_fma_f32 v30, -v88, v89, 1.0
	v_fmac_f32_e32 v89, v30, v89
	v_div_scale_f32 v30, vcc, 1.0, v81, 1.0
	v_mul_f32_e32 v31, v30, v89
	v_pk_mul_f32 v[86:87], v[32:33], v[82:83] op_sel_hi:[0,1]
	v_pk_fma_f32 v[4:5], v[32:33], v[82:83], v[4:5] op_sel_hi:[0,1,1]
	v_fma_f32 v32, -v88, v31, v30
	v_fmac_f32_e32 v31, v32, v89
	v_fma_f32 v30, -v88, v31, v30
	v_div_fmas_f32 v30, v30, v89, v31
	v_div_fixup_f32 v30, v30, v81, 1.0
	v_pk_fma_f32 v[82:83], v[30:31], v[4:5], v[86:87] op_sel_hi:[0,1,1] neg_lo:[0,0,1] neg_hi:[0,0,1]
	v_pk_fma_f32 v[30:31], v[30:31], v[6:7], v[84:85] op_sel_hi:[0,1,1] neg_lo:[0,0,1] neg_hi:[0,0,1]
	v_pk_mul_f32 v[30:31], v[2:3], v[30:31]
	v_pk_mul_f32 v[82:83], v[0:1], v[82:83]
	s_nop 0
	v_cvt_pk_bf16_f32 v82, v82, v83
	v_cvt_pk_bf16_f32 v83, v30, v31
	v_lshl_add_u64 v[30:31], s[50:51], 0, v[14:15]
	global_store_dwordx2 v[30:31], v[82:83], off
	v_add_u32_e32 v30, s35, v38
	s_and_saveexec_b64 s[66:67], s[22:23]
	s_cbranch_execz .LBB0_316
	ds_read_b32 v32, v30 offset:4
	v_xor_b32_e32 v81, 0x80000000, v80
	v_xor_b32_e32 v80, 0x80000000, v79
	v_xor_b32_e32 v79, 0x80000000, v78
	v_xor_b32_e32 v78, 0x80000000, v76
	s_waitcnt lgkmcnt(0)
	v_pk_fma_f32 v[6:7], v[80:81], v[32:33], v[6:7] op_sel_hi:[1,0,1]
	v_pk_fma_f32 v[4:5], v[78:79], v[32:33], v[4:5] op_sel_hi:[1,0,1]
